# scan: compute waves at static s_setprio 1 over the loader wave on their SIMD
# baseline (speedup 1.0000x reference)
; #define LDS_BARRIER() do { asm volatile("s_waitcnt lgkmcnt(0)" ::: "memory"); __builtin_amdgcn_s_barrier(); asm volatile("" ::: "memory"); } while (0)
; __device__ __forceinline__ void p4_scan(const Args& a, const Frame& F) {
;     ...
;             int c = lane & 15, q = lane >> 4; asm volatile("" : "+v"(c), "+v"(q));
;             const int ta = w, tb = 7 - w, trA = 16 * ta + c, trB = 16 * tb + c;
;             unsigned kadA[8];
; #pragma unroll
;             for (int ks = 0; ks < 4; ++ks)
; #pragma unroll
;                 for (int t = 0; t < 2; ++t) kadA[ks * 2 + t] = (unsigned)((32 * ks + 8 * q + 4 * t + (c >> 2)) * SP + (4 * w + ((c & 3) >> 1)) * 16 + 8 * (c & 1));
;             f32x4 accC[2][3];
; #pragma unroll
;             for (int d2 = 0; d2 < 2; ++d2)
; #pragma unroll
;                 for (int i = 0; i < 3; ++i) accC[d2][i] = (f32x4){0.f, 0.f, 0.f, 0.f};
;             float mcar = 0.f, pbt, ppx;
;             { const int base0 = chunk_base(0); pbt = CH[(hd * 528 + (base0 >> 7)) * 2]; ppx = CH[(hd * 528 + (base0 >> 7)) * 2 + 1]; }
;             LDS_BARRIER();
;             float btot = pbt, pmx = ppx;
;             LDS_BARRIER();
;             const int npA = (ta + 2) >> 1, npB = (tb + 2) >> 1;
.LBB0_447:
	s_or_b64 exec, exec, s[10:11]
	s_lshl_b32 s56, s97, 2
	s_and_b32 s4, s56, 28
	s_ashr_i32 s5, s97, 6
	s_add_i32 s4, s4, s5
	s_bfe_u32 s59, s97, 0x10005
	s_and_b32 s55, s5, 3
	s_ashr_i32 s58, s4, 2
	s_lshl_b32 s4, s59, 2
	s_bfe_u32 s54, s97, 0x20003
	s_or_b32 s57, s4, s55
	s_cmp_eq_u32 s59, 0
	s_mov_b64 s[6:7], -1
	s_cselect_b64 s[4:5], -1, 0
	s_and_b64 vcc, exec, s[40:41]
	s_mul_i32 s76, s57, 0x210
	s_cbranch_vccz .LBB0_473
	v_mov_b32_e32 v9, v154
	v_mov_b32_e32 v10, v155
	s_and_b64 s[6:7], s[4:5], exec
	v_lshlrev_b32_e32 v11, 3, v10
	v_lshrrev_b32_e32 v8, 2, v9
	v_add_u32_e32 v12, v8, v11
	v_lshlrev_b32_e32 v8, 3, v9
	s_mov_b32 s6, 0xac00000
	v_and_or_b32 v8, v8, 24, s67
	s_cselect_b32 s77, s6, 0xec00000
	v_mad_u64_u32 v[148:149], s[6:7], v12, s84, v[8:9]
	s_lshl_b32 s87, s58, 8
	s_add_i32 s87, s87, 0x10000
	s_lshl_b32 s6, s59, 7
	s_or_b32 s8, s87, s6
	s_ashr_i32 s6, s8, 7
	s_add_i32 s6, s6, s76
	s_lshl_b32 s6, s6, 1
	s_ashr_i32 s7, s6, 31
	s_lshl_b64 s[6:7], s[6:7], 2
	s_add_u32 s6, s60, s6
	s_addc_u32 s7, s61, s7
	global_load_dwordx2 v[152:153], v145, s[6:7]
	v_add_u32_e32 v147, s65, v9
	v_add_u32_e32 v177, s66, v9
	v_mul_lo_u32 v8, v147, s84
	v_add_u32_e32 v33, 0, v8
	v_mul_lo_u32 v8, v177, s84
	v_lshlrev_b32_e32 v178, 4, v10
	v_add_u32_e32 v34, 0, v8
	v_lshlrev_b32_e32 v8, 2, v147
	v_add_u32_e32 v179, s85, v8
	v_lshlrev_b32_e32 v12, 2, v177
	v_add_u32_e32 v181, s89, v8
	v_lshlrev_b32_e32 v184, 2, v10
	v_add_u32_e32 v8, v178, v9
	v_and_b32_e32 v10, 3, v9
	v_add_u32_e32 v180, s85, v12
	v_add_u32_e32 v182, s89, v12
	v_bfe_u32 v8, v8, 2, 4
	v_lshlrev_b32_e32 v12, 6, v10
	v_lshl_or_b32 v185, v8, 2, v12
	v_or_b32_e32 v12, s65, v8
	s_waitcnt lgkmcnt(0)
	s_barrier
	v_sub_u32_e32 v13, 0x7f, v12
	v_or_b32_e32 v8, s66, v8
	s_waitcnt lgkmcnt(0)
	s_barrier
	s_add_i32 s6, 0, 0x20130
	v_and_b32_e32 v36, 63, v9
	v_cndmask_b32_e64 v186, v13, v12, s[4:5]
	v_sub_u32_e32 v12, 0x7f, v8
	v_lshlrev_b32_e32 v32, 2, v10
	v_mul_lo_u32 v188, v9, s84
	v_add_u32_e32 v35, s6, v178
	v_add_u32_e32 v183, 0, v178
	v_cndmask_b32_e64 v187, v12, v8, s[4:5]
	s_lshl_b32 s6, s55, 7
	s_lshl_b32 s7, s54, 5
	v_add_u32_e32 v37, s80, v11
	v_add_u32_e32 v8, v188, v178
	v_lshlrev_b32_e32 v144, 1, v32
	v_and_or_b32 v32, v162, 64, v36
	s_mov_b32 s11, 0
	v_add_u32_e32 v149, 0x440, v148
	v_add_u32_e32 v171, 0x2200, v148
	v_add_u32_e32 v172, 0x2640, v148
	v_add_u32_e32 v173, 0x4400, v148
	v_add_u32_e32 v174, 0x4840, v148
	v_add_u32_e32 v175, 0x6600, v148
	v_add_u32_e32 v176, 0x6a40, v148
	s_lshl_b32 s33, s58, 13
	s_xor_b32 s88, s8, 0x80
	v_add_u32_e32 v189, v183, v188
	v_add3_u32 v190, s82, v188, v11
	v_add3_u32 v191, s83, v188, v11
	v_add_u32_e32 v192, 0x2200, v8
	v_add_u32_e32 v193, s90, v8
	v_mov_b32_e32 v201, 0
	v_mov_b32_e32 v8, 0
	v_mov_b32_e32 v9, 0
	v_mov_b32_e32 v10, 0
	v_mov_b32_e32 v11, 0
	v_mov_b32_e32 v12, 0
	v_mov_b32_e32 v13, 0
	v_mov_b32_e32 v14, 0
	v_mov_b32_e32 v15, 0
	v_mov_b32_e32 v16, 0
	v_mov_b32_e32 v17, 0
	v_mov_b32_e32 v18, 0
	v_mov_b32_e32 v19, 0
	v_mov_b32_e32 v20, 0
	v_mov_b32_e32 v21, 0
	v_mov_b32_e32 v22, 0
	v_mov_b32_e32 v23, 0
	v_mov_b32_e32 v24, 0
	v_mov_b32_e32 v25, 0
	v_mov_b32_e32 v26, 0
	v_mov_b32_e32 v27, 0
	v_mov_b32_e32 v28, 0
	v_mov_b32_e32 v29, 0
	v_mov_b32_e32 v30, 0
	v_mov_b32_e32 v31, 0
	v_add_u32_e32 v194, v33, v178
	v_add_u32_e32 v195, v34, v178
	v_add_u32_e32 v196, v35, v188
	s_lshl_b32 s44, s6, 1
	s_lshl_b32 s10, s7, 1
	v_add_u32_e32 v197, v37, v188
	v_lshlrev_b32_e32 v200, 2, v32
	s_waitcnt vmcnt(0)
	s_setprio 1
	s_branch .LBB0_450

; __device__ __forceinline__ unsigned xb_ld(unsigned* p)              { return __hip_atomic_load(p, __ATOMIC_RELAXED, __HIP_MEMORY_SCOPE_AGENT); }
; __device__ __forceinline__ void xcd_barrier_complete(unsigned* bar, unsigned x, unsigned& nloc, unsigned& nx) {
;     const unsigned G = gridDim.x * gridDim.y * gridDim.z;
;     unsigned sum, cnt, mine, sp = 0u;
;     for (;;) {
;         sum = 0u; cnt = 0u; mine = 0u;
; #pragma unroll
;         for (unsigned j = 0; j < 16; ++j) { const unsigned c = xb_ld(&bar[XB_XCNT(j)]); sum += c; cnt += (c > 0u) ? 1u : 0u; mine = (j == x) ? c : mine; }
;         if (sum == G) break;
;         __builtin_amdgcn_s_sleep(1);
;         if ((++sp & 255u) == 0u) { if (xb_ld(&bar[XB_TMO])) break; if (sp > XB_SPIN_CAP) { atomicAdd(&bar[XB_TMO], 1u); break; } }
;     }
; __device__ __forceinline__ void xcd_barrier(const XcdBarrier& b) {
;     asm volatile("s_waitcnt vmcnt(0)" ::: "memory");
;     __syncthreads();
;     if (threadIdx.x == 0) {
;         unsigned* bar = b.bar;
;         __builtin_amdgcn_s_waitcnt(0);
;         unsigned nloc = b.st[0], nx = b.st[1];
;         if (nloc == 0u) { xcd_barrier_complete(bar, b.x, nloc, nx); b.st[0] = nloc; b.st[1] = nx; }
.LBB0_511:
	s_setprio 0
	s_cmp_gt_i32 s75, 5
	s_cselect_b64 s[0:1], -1, 0
	s_and_b64 s[4:5], s[14:15], s[0:1]
	s_andn2_b64 vcc, exec, s[4:5]
	s_cbranch_vccnz .LBB0_561
	s_waitcnt vmcnt(0)
	v_cmp_eq_u32_e32 vcc, 0, v0
	s_waitcnt vmcnt(0) lgkmcnt(0)
	s_barrier
	s_and_saveexec_b64 s[4:5], vcc
	s_cbranch_execz .LBB0_560
	v_readlane_b32 s6, v255, 2
	s_waitcnt vmcnt(0) expcnt(0) lgkmcnt(0)
	s_nop 0
	v_mov_b32_e32 v1, s6
	ds_read_b32 v3, v1
	ds_read_b32 v1, v1 offset:4
	s_waitcnt lgkmcnt(1)
	v_cmp_ne_u32_e32 vcc, 0, v3
	s_cbranch_vccnz .LBB0_528
	v_readlane_b32 s6, v255, 0
	v_readlane_b32 s7, v255, 1
	s_load_dwordx2 s[10:11], s[6:7], 0x4
	s_add_u32 s6, s72, 0x4200
	s_addc_u32 s7, s73, 0
	s_add_u32 s8, s72, 0x4400
	s_addc_u32 s9, s73, 0
	s_waitcnt lgkmcnt(0)
	s_mul_i32 s33, s10, s3
	s_add_u32 s10, s72, 0x4500
	s_mul_i32 s33, s33, s11
	s_addc_u32 s11, s73, 0
	s_add_u32 s12, s72, 0x4600
	s_addc_u32 s13, s73, 0
	s_add_u32 s14, s72, 0x4700
	s_addc_u32 s15, s73, 0
	s_add_u32 s16, s72, 0x4800
	s_addc_u32 s17, s73, 0
	s_add_u32 s20, s72, 0x4900
	s_addc_u32 s21, s73, 0
	s_add_u32 s24, s72, 0x4a00
	s_addc_u32 s25, s73, 0
	s_add_u32 s28, s72, 0x4b00
	s_addc_u32 s29, s73, 0
	s_add_u32 s38, s72, 0x4c00
	s_addc_u32 s39, s73, 0
	s_add_u32 s40, s72, 0x4d00
	s_addc_u32 s41, s73, 0
	s_add_u32 s42, s72, 0x4e00
	s_addc_u32 s43, s73, 0
	s_add_u32 s44, s72, 0x4f00
	s_addc_u32 s45, s73, 0
	s_add_u32 s46, s72, 0x5000
	s_addc_u32 s47, s73, 0
	s_add_u32 s48, s72, 0x5100
	s_addc_u32 s49, s73, 0
	s_add_u32 s50, s72, 0x5200
	s_addc_u32 s51, s73, 0
	s_add_u32 s52, s72, 0x5300
	s_addc_u32 s53, s73, 0
	s_mov_b32 s34, 1
	v_mov_b32_e32 v17, 0
	s_branch .LBB0_516
